# speedup vs baseline: 1.0064x; 1.0064x over previous
.LBB0_95:
	s_lshl_b32 s94, s97, 4
	v_add_u32_e32 v2, s94, v79
	v_cmp_gt_i32_e32 vcc, s100, v2
	v_add_u32_e32 v2, s98, v2
	s_mov_b64 s[30:31], vcc
	v_cndmask_b32_e32 v2, 0, v2, vcc
	v_lshlrev_b32_e32 v108, 2, v2
	v_cmp_lt_i32_e32 vcc, -1, v55
	v_lshl_add_u32 v2, v55, 8, v70
	s_mov_b64 s[90:91], vcc
	v_cndmask_b32_e32 v2, v70, v2, vcc
	s_cmp_lt_i32 s86, s68
	s_cselect_b64 s[78:79], -1, 0
	s_lshl_b32 s94, s81, 4
	s_add_i32 s95, s94, 16
	s_cmp_ge_i32 s95, s83
	s_cselect_b64 s[0:1], -1, 0
	s_waitcnt vmcnt(0)
	v_mov_b64_e32 v[66:67], v[74:75]
	v_mov_b64_e32 v[68:69], v[76:77]
	v_mov_b64_e32 v[62:63], v[94:95]
	v_mov_b64_e32 v[64:65], v[96:97]
	v_mov_b64_e32 v[58:59], v[120:121]
	v_mov_b64_e32 v[60:61], v[122:123]
	v_mov_b64_e32 v[54:55], v[124:125]
	v_mov_b64_e32 v[56:57], v[126:127]
	s_cbranch_scc0 .Lattn_noqcopy
	v_mov_b32_e32 v99, v80
	v_mov_b32_e32 v100, v81
	v_mov_b32_e32 v101, v82
	v_mov_b32_e32 v102, v83
.Lattn_noqcopy:
	s_lshl_b32 s95, s87, 4
	s_add_i32 s95, s95, 16
	s_cmp_lt_i32 s95, s88
	s_cbranch_scc1 .LBB0_97
	s_cmp_ge_i32 s96, s68
	s_cbranch_scc1 .LBB0_97
	s_lshl_b32 s95, s96, 1
	v_mov_b32_e32 v104, s95
	v_or_b32_e32 v105, 1, v104
	v_min_i32_e32 v105, s67, v105
	v_cndmask_b32_e64 v104, v105, v104, s[38:39]
	v_add_u32_e32 v104, s66, v104
	v_ashrrev_i32_e32 v105, 31, v104
	v_lshlrev_b64 v[104:105], 8, v[104:105]
	v_lshl_add_u64 v[104:105], v[72:73], 0, v[104:105]
	global_load_dwordx4 v[80:83], v[104:105], off nt
.LBB0_97:
	global_load_dword v98, v108, s[58:59]
	global_load_dwordx4 v[74:77], v2, s[92:93]
	global_load_dwordx4 v[94:97], v2, s[92:93] offset:64
	global_load_dwordx4 v[120:123], v2, s[92:93] offset:128
	global_load_dwordx4 v[124:127], v2, s[92:93] offset:192
	s_cmp_lt_i32 s80, 0
	s_cbranch_scc1 .Lattn_skip
	v_mfma_f32_16x16x32_f16 v[104:107], v[66:69], v[6:9], 0
	v_or_b32_e32 v2, s94, v79
	v_cmp_lt_i32_e64 s[42:43], v2, s82
	v_cmp_ge_i32_e64 s[40:41], v2, s82
	v_mfma_f32_16x16x32_f16 v[104:107], v[62:65], v[10:13], v[104:107]
	s_and_b64 s[42:43], s[84:85], s[42:43]
	v_cndmask_b32_e64 v2, 0, 1, s[42:43]
	s_and_b64 s[40:41], s[40:41], s[84:85]
	v_cmp_ne_u32_e64 s[42:43], 0, v2
	v_cndmask_b32_e64 v2, 0, 1, s[40:41]
	v_mfma_f32_16x16x32_f16 v[104:107], v[58:61], v[14:17], v[104:107]
	v_cmp_ne_u32_e32 vcc, 0, v2
	v_mov_b32_e32 v5, s42
	v_cmp_ngt_f32_e64 s[48:49], s70, v103
	v_mov_b32_e32 v2, vcc_lo
	v_cndmask_b32_e64 v2, v2, v5, s[38:39]
	v_mfma_f32_16x16x32_f16 v[108:111], v[54:57], v[18:21], v[104:107]
	v_lshrrev_b32_sdwa v2, v88, v2 dst_sel:DWORD dst_unused:UNUSED_PAD src0_sel:DWORD src1_sel:WORD_0
	v_and_b32_e32 v5, 1, v2
	v_cmp_eq_u32_e64 s[46:47], 0, v5
	v_and_b32_e32 v5, 2, v2
	v_cmp_eq_u32_e64 s[40:41], 0, v5
	v_and_b32_e32 v104, 4, v2
	v_and_b32_e32 v2, 8, v2
	s_nop 0
	v_cndmask_b32_e64 v107, v108, v71, s[46:47]
	v_cndmask_b32_e64 v105, v109, v71, s[40:41]
	v_cmp_eq_u32_e64 s[42:43], 0, v104
	v_cmp_eq_u32_e64 s[44:45], 0, v2
	v_max3_f32 v5, v107, s69, v105
	v_cndmask_b32_e64 v106, v110, v71, s[42:43]
	v_cndmask_b32_e64 v104, v111, v71, s[44:45]
	v_max3_f32 v2, v5, v106, v104
	v_mov_b32_e32 v5, v2
	s_nop 1
	v_permlane16_swap_b32_e32 v5, v2
	v_max_f32_e32 v2, v2, v5
	v_mov_b32_e32 v5, v2
	s_nop 1
	v_permlane32_swap_b32_e32 v5, v2
	v_max_f32_e32 v108, v2, v5
	v_sub_f32_e32 v2, v108, v103
	v_cmp_lt_f32_e32 vcc, s71, v2
	s_and_b64 vcc, s[48:49], vcc
	s_nop 0
	v_cndmask_b32_e64 v2, 0, 1, vcc
	v_cmp_ne_u32_e64 s[50:51], 0, v2
	s_cmp_lg_u64 s[50:51], 0
	s_cselect_b64 s[50:51], -1, 0
	s_cbranch_vccz .LBB0_117
	v_max_f32_e32 v2, v108, v108
	v_max_f32_e32 v5, v103, v103
	v_max_f32_e32 v5, v5, v2
	v_sub_f32_e32 v2, v103, v5
	v_exp_f32_e32 v2, v2
	s_cbranch_execnz .LBB0_100

.Lattn_g_done:
	s_and_saveexec_b64 s[40:41], s[0:1]
	s_cbranch_execz .LBB0_108
	v_mov_b32_e32 v2, v54
	s_nop 1
	v_permlane16_swap_b32_e32 v2, v54
	v_add_f32_e32 v54, v54, v2
	v_mov_b32_e32 v55, v54
	s_nop 1
	v_permlane32_swap_b32_e32 v55, v54
	s_lshl_b32 s95, s80, 1
	v_mov_b32_e32 v2, s95
	v_or_b32_e32 v4, 1, v2
	v_cmp_gt_i32_e32 vcc, s33, v4
	ds_read_b128 v[4:7], v86 offset:32768
	ds_read_b128 v[8:11], v86 offset:33792
	ds_read_b128 v[12:15], v86 offset:34816
	ds_read_b128 v[16:19], v86 offset:35840
	v_cvt_pk_f16_f32 v53, v52, v53
	v_cvt_pk_f16_f32 v52, v50, v51
	v_cvt_pk_f16_f32 v51, v48, v49
	v_cvt_pk_f16_f32 v50, v46, v47
	v_cvt_pk_f16_f32 v45, v44, v45
	v_cvt_pk_f16_f32 v44, v42, v43
	v_cvt_pk_f16_f32 v43, v40, v41
	v_cvt_pk_f16_f32 v42, v38, v39
	v_cvt_pk_f16_f32 v37, v36, v37
	v_cvt_pk_f16_f32 v36, v34, v35
	v_cvt_pk_f16_f32 v35, v32, v33
	v_cvt_pk_f16_f32 v34, v30, v31
	ds_read_b128 v[30:33], v86 offset:36864
	ds_read_b128 v[38:41], v86 offset:37888
	ds_read_b128 v[46:49], v86 offset:38912
	ds_read_b128 v[56:59], v86 offset:39936
	v_cvt_pk_f16_f32 v63, v28, v29
	v_cvt_pk_f16_f32 v62, v26, v27
	v_cvt_pk_f16_f32 v61, v24, v25
	v_cvt_pk_f16_f32 v60, v22, v23
	s_waitcnt lgkmcnt(7)
	v_mfma_f32_16x16x32_f16 v[4:7], v[4:7], v[50:53], 0
	s_waitcnt lgkmcnt(6)
	v_mfma_f32_16x16x32_f16 v[4:7], v[8:11], v[42:45], v[4:7]
	s_waitcnt lgkmcnt(5)
	v_mfma_f32_16x16x32_f16 v[4:7], v[12:15], v[34:37], v[4:7]
	s_waitcnt lgkmcnt(4)
	v_mfma_f32_16x16x32_f16 v[12:15], v[16:19], v[60:63], v[4:7]
	ds_read_b128 v[8:11], v86 offset:44032
	ds_read_b128 v[16:19], v86 offset:43008
	ds_read_b128 v[20:23], v86 offset:41984
	ds_read_b128 v[24:27], v86 offset:40960
	s_waitcnt lgkmcnt(7)
	v_mfma_f32_16x16x32_f16 v[4:7], v[30:33], v[50:53], 0
	s_waitcnt lgkmcnt(6)
	v_mfma_f32_16x16x32_f16 v[4:7], v[38:41], v[42:45], v[4:7]
	s_waitcnt lgkmcnt(5)
	v_mfma_f32_16x16x32_f16 v[4:7], v[46:49], v[34:37], v[4:7]
	s_waitcnt lgkmcnt(4)
	v_mfma_f32_16x16x32_f16 v[4:7], v[56:59], v[60:63], v[4:7]
	ds_read_b128 v[28:31], v86 offset:45056
	ds_read_b128 v[38:41], v86 offset:46080
	ds_read_b128 v[46:49], v86 offset:47104
	ds_read_b128 v[56:59], v86 offset:48128
	s_waitcnt lgkmcnt(4)
	v_mfma_f32_16x16x32_f16 v[24:27], v[24:27], v[50:53], 0
	v_mfma_f32_16x16x32_f16 v[20:23], v[20:23], v[42:45], v[24:27]
	v_mfma_f32_16x16x32_f16 v[16:19], v[16:19], v[34:37], v[20:23]
	v_mfma_f32_16x16x32_f16 v[8:11], v[8:11], v[60:63], v[16:19]
	s_nop 5
	ds_read_b128 v[20:23], v86 offset:52224
	ds_read_b128 v[24:27], v86 offset:51200
	ds_read_b128 v[64:67], v86 offset:50176
	ds_read_b128 v[104:107], v86 offset:49152
	s_waitcnt lgkmcnt(7)
	v_mfma_f32_16x16x32_f16 v[16:19], v[28:31], v[50:53], 0
	s_waitcnt lgkmcnt(6)
	v_mfma_f32_16x16x32_f16 v[16:19], v[38:41], v[42:45], v[16:19]
	s_waitcnt lgkmcnt(5)
	v_mfma_f32_16x16x32_f16 v[16:19], v[46:49], v[34:37], v[16:19]
	s_waitcnt lgkmcnt(4)
	v_mfma_f32_16x16x32_f16 v[16:19], v[56:59], v[60:63], v[16:19]
	ds_read_b128 v[28:31], v86 offset:53248
	ds_read_b128 v[38:41], v86 offset:54272
	ds_read_b128 v[46:49], v86 offset:55296
	ds_read_b128 v[56:59], v86 offset:56320
	s_waitcnt lgkmcnt(4)
	v_mfma_f32_16x16x32_f16 v[104:107], v[104:107], v[50:53], 0
	v_mfma_f32_16x16x32_f16 v[64:67], v[64:67], v[42:45], v[104:107]
	v_mfma_f32_16x16x32_f16 v[24:27], v[24:27], v[34:37], v[64:67]
	v_mfma_f32_16x16x32_f16 v[20:23], v[20:23], v[60:63], v[24:27]
	s_nop 5
	ds_read_b128 v[64:67], v86 offset:60416
	ds_read_b128 v[104:107], v86 offset:59392
	ds_read_b128 v[108:111], v86 offset:58368
	ds_read_b128 v[112:115], v86 offset:57344
	s_waitcnt lgkmcnt(7)
	v_mfma_f32_16x16x32_f16 v[24:27], v[28:31], v[50:53], 0
	s_waitcnt lgkmcnt(6)
	v_mfma_f32_16x16x32_f16 v[24:27], v[38:41], v[42:45], v[24:27]
	s_waitcnt lgkmcnt(5)
	v_mfma_f32_16x16x32_f16 v[24:27], v[46:49], v[34:37], v[24:27]
	s_waitcnt lgkmcnt(4)
	v_mfma_f32_16x16x32_f16 v[24:27], v[56:59], v[60:63], v[24:27]
	ds_read_b128 v[38:41], v86 offset:61440
	ds_read_b128 v[46:49], v86 offset:62464
	ds_read_b128 v[56:59], v86 offset:63488
	ds_read_b128 v[116:119], v86 offset:64512
	s_waitcnt lgkmcnt(4)
	v_mfma_f32_16x16x32_f16 v[28:31], v[112:115], v[50:53], 0
	v_mfma_f32_16x16x32_f16 v[28:31], v[108:111], v[42:45], v[28:31]
	v_mfma_f32_16x16x32_f16 v[28:31], v[104:107], v[34:37], v[28:31]
	v_mfma_f32_16x16x32_f16 v[28:31], v[64:67], v[60:63], v[28:31]
	s_waitcnt lgkmcnt(3)
	v_mfma_f32_16x16x32_f16 v[38:41], v[38:41], v[50:53], 0
	s_waitcnt lgkmcnt(2)
	v_mfma_f32_16x16x32_f16 v[38:41], v[46:49], v[42:45], v[38:41]
	s_waitcnt lgkmcnt(1)
	v_mfma_f32_16x16x32_f16 v[32:35], v[56:59], v[34:37], v[38:41]
	s_waitcnt lgkmcnt(0)
	v_mfma_f32_16x16x32_f16 v[32:35], v[116:119], v[60:63], v[32:35]
	s_or_b64 s[42:43], s[38:39], vcc
	s_and_saveexec_b64 s[0:1], s[42:43]
	s_cbranch_execz .LBB0_105
	v_lshlrev_b32_e32 v36, 1, v78
	ds_read_b128 v[36:39], v36 offset:27472
	v_cndmask_b32_e64 v12, 0, v12, s[14:15]
	v_cndmask_b32_e64 v13, 0, v13, s[14:15]
	v_cndmask_b32_e64 v14, 0, v14, s[14:15]
	v_cndmask_b32_e64 v15, 0, v15, s[14:15]
	v_cndmask_b32_e64 v7, v15, v7, s[12:13]
	v_cndmask_b32_e64 v6, v14, v6, s[12:13]
	v_cndmask_b32_e64 v5, v13, v5, s[12:13]
	v_cndmask_b32_e64 v4, v12, v4, s[12:13]
	v_add_f32_e32 v40, v54, v55
	v_cndmask_b32_e64 v4, v4, v8, s[10:11]
	v_cndmask_b32_e64 v5, v5, v9, s[10:11]
	v_cndmask_b32_e64 v6, v6, v10, s[10:11]
	v_cndmask_b32_e64 v7, v7, v11, s[10:11]
	v_rcp_f32_e32 v12, v40
	v_cndmask_b32_e64 v7, v7, v19, s[8:9]
	v_cndmask_b32_e64 v6, v6, v18, s[8:9]
	v_cndmask_b32_e64 v5, v5, v17, s[8:9]
	v_cndmask_b32_e64 v4, v4, v16, s[8:9]
	v_cndmask_b32_e64 v4, v4, v20, s[6:7]
	v_cndmask_b32_e64 v5, v5, v21, s[6:7]
	v_cndmask_b32_e64 v6, v6, v22, s[6:7]
	v_cndmask_b32_e64 v7, v7, v23, s[6:7]
	v_cndmask_b32_e64 v7, v7, v27, s[20:21]
	v_cndmask_b32_e64 v6, v6, v26, s[20:21]
	v_cndmask_b32_e64 v5, v5, v25, s[20:21]
	v_cndmask_b32_e64 v4, v4, v24, s[20:21]
	v_cmp_lt_f32_e32 vcc, 0, v40
	v_cndmask_b32_e64 v4, v4, v28, s[18:19]
	v_cndmask_b32_e64 v5, v5, v29, s[18:19]
	v_cndmask_b32_e64 v6, v6, v30, s[18:19]
	v_cndmask_b32_e64 v7, v7, v31, s[18:19]
	v_cndmask_b32_e32 v8, 0, v12, vcc
	v_cndmask_b32_e64 v7, v7, v35, s[16:17]
	v_cndmask_b32_e64 v6, v6, v34, s[16:17]
	v_cndmask_b32_e64 v5, v5, v33, s[16:17]
	v_cndmask_b32_e64 v4, v4, v32, s[16:17]
	v_or_b32_e32 v2, v2, v89
	s_waitcnt lgkmcnt(0)
	v_fma_mixlo_f16 v4, v8, v4, v36
	v_fma_mixlo_f16 v5, v8, v5, v37
	v_fma_mixlo_f16 v6, v8, v6, v38
	v_fma_mixlo_f16 v7, v8, v7, v39
	v_cndmask_b32_e32 v4, 0, v4, vcc
	v_cndmask_b32_e32 v8, 0, v5, vcc
	v_cndmask_b32_e32 v5, 0, v6, vcc
	v_cndmask_b32_e32 v6, 0, v7, vcc
	v_pack_b32_f16 v5, v5, v6
	v_pack_b32_f16 v4, v4, v8
	v_mad_u64_u32 v[6:7], s[42:43], v2, s72, v[78:79]
	ds_write_b64 v6, v[4:5]
